# B-fragment LDS base hoist extended to all six GEMM K-loops (P2,P6,P8,P12,P17,P19); on top of v062
# baseline (speedup 1.0000x reference)
.LBB0_494:
	s_ashr_i32 s17, s16, 31
	v_cmp_lt_i64_e32 vcc, s[18:19], v[174:175]
	s_lshl_b64 s[18:19], s[16:17], 19
	v_readlane_b32 s6, v254, 36
	s_add_u32 s18, s6, s18
	v_readlane_b32 s6, v254, 37
	s_addc_u32 s19, s6, s19
	s_and_b64 s[20:21], vcc, exec
	s_cselect_b32 s6, s19, s27
	s_cselect_b32 s17, s18, s26
	s_ashr_i32 s15, s14, 31
	s_lshl_b64 s[20:21], s[14:15], 19
	s_add_u32 s20, s13, s20
	s_addc_u32 s21, s33, s21
	s_and_b64 s[30:31], vcc, exec
	s_cselect_b32 s15, s21, s29
	s_cselect_b32 s49, s20, s28
	s_add_u32 s26, s26, 0x40080
	s_addc_u32 s27, s27, 0
	s_add_u32 s50, s28, 0x100
	v_mov_b32_e32 v18, 0
	s_addc_u32 s51, s29, 0
	s_mov_b32 s52, -2
	v_mov_b32_e32 v19, v18
	v_mov_b32_e32 v20, v18
	v_mov_b32_e32 v21, v18
	v_mov_b32_e32 v22, v18
	v_mov_b32_e32 v23, v18
	v_mov_b32_e32 v24, v18
	v_mov_b32_e32 v25, v18
	v_mov_b32_e32 v34, v18
	v_mov_b32_e32 v35, v18
	v_mov_b32_e32 v36, v18
	v_mov_b32_e32 v37, v18
	v_mov_b32_e32 v38, v18
	v_mov_b32_e32 v39, v18
	v_mov_b32_e32 v40, v18
	v_mov_b32_e32 v41, v18
	v_mov_b32_e32 v50, v18
	v_mov_b32_e32 v51, v18
	v_mov_b32_e32 v52, v18
	v_mov_b32_e32 v53, v18
	v_mov_b32_e32 v54, v18
	v_mov_b32_e32 v55, v18
	v_mov_b32_e32 v56, v18
	v_mov_b32_e32 v57, v18
	v_mov_b32_e32 v66, v18
	v_mov_b32_e32 v67, v18
	v_mov_b32_e32 v68, v18
	v_mov_b32_e32 v69, v18
	v_mov_b32_e32 v70, v18
	v_mov_b32_e32 v71, v18
	v_mov_b32_e32 v72, v18
	v_mov_b32_e32 v73, v18
	v_mov_b32_e32 v26, v18
	v_mov_b32_e32 v27, v18
	v_mov_b32_e32 v28, v18
	v_mov_b32_e32 v29, v18
	v_mov_b32_e32 v30, v18
	v_mov_b32_e32 v31, v18
	v_mov_b32_e32 v32, v18
	v_mov_b32_e32 v33, v18
	v_mov_b32_e32 v42, v18
	v_mov_b32_e32 v43, v18
	v_mov_b32_e32 v44, v18
	v_mov_b32_e32 v45, v18
	v_mov_b32_e32 v46, v18
	v_mov_b32_e32 v47, v18
	v_mov_b32_e32 v48, v18
	v_mov_b32_e32 v49, v18
	v_mov_b32_e32 v58, v18
	v_mov_b32_e32 v59, v18
	v_mov_b32_e32 v60, v18
	v_mov_b32_e32 v61, v18
	v_mov_b32_e32 v62, v18
	v_mov_b32_e32 v63, v18
	v_mov_b32_e32 v64, v18
	v_mov_b32_e32 v65, v18
	v_mov_b32_e32 v74, v18
	v_mov_b32_e32 v75, v18
	v_mov_b32_e32 v76, v18
	v_mov_b32_e32 v77, v18
	v_mov_b32_e32 v78, v18
	v_mov_b32_e32 v79, v18
	v_mov_b32_e32 v80, v18
	v_mov_b32_e32 v81, v18
	v_mov_b32_e32 v82, v18
	v_mov_b32_e32 v83, v18
	v_mov_b32_e32 v84, v18
	v_mov_b32_e32 v85, v18
	v_mov_b32_e32 v86, v18
	v_mov_b32_e32 v87, v18
	v_mov_b32_e32 v88, v18
	v_mov_b32_e32 v89, v18
	v_mov_b32_e32 v98, v18
	v_mov_b32_e32 v99, v18
	v_mov_b32_e32 v100, v18
	v_mov_b32_e32 v101, v18
	v_mov_b32_e32 v102, v18
	v_mov_b32_e32 v103, v18
	v_mov_b32_e32 v104, v18
	v_mov_b32_e32 v105, v18
	v_mov_b32_e32 v114, v18
	v_mov_b32_e32 v115, v18
	v_mov_b32_e32 v116, v18
	v_mov_b32_e32 v117, v18
	v_mov_b32_e32 v118, v18
	v_mov_b32_e32 v119, v18
	v_mov_b32_e32 v120, v18
	v_mov_b32_e32 v121, v18
	v_mov_b32_e32 v130, v18
	v_mov_b32_e32 v131, v18
	v_mov_b32_e32 v132, v18
	v_mov_b32_e32 v133, v18
	v_mov_b32_e32 v134, v18
	v_mov_b32_e32 v135, v18
	v_mov_b32_e32 v136, v18
	v_mov_b32_e32 v137, v18
	v_mov_b32_e32 v90, v18
	v_mov_b32_e32 v91, v18
	v_mov_b32_e32 v92, v18
	v_mov_b32_e32 v93, v18
	v_mov_b32_e32 v94, v18
	v_mov_b32_e32 v95, v18
	v_mov_b32_e32 v96, v18
	v_mov_b32_e32 v97, v18
	v_mov_b32_e32 v106, v18
	v_mov_b32_e32 v107, v18
	v_mov_b32_e32 v108, v18
	v_mov_b32_e32 v109, v18
	v_mov_b32_e32 v110, v18
	v_mov_b32_e32 v111, v18
	v_mov_b32_e32 v112, v18
	v_mov_b32_e32 v113, v18
	v_mov_b32_e32 v122, v18
	v_mov_b32_e32 v123, v18
	v_mov_b32_e32 v124, v18
	v_mov_b32_e32 v125, v18
	v_mov_b32_e32 v126, v18
	v_mov_b32_e32 v127, v18
	v_mov_b32_e32 v128, v18
	v_mov_b32_e32 v129, v18
	v_mov_b32_e32 v138, v18
	v_mov_b32_e32 v139, v18
	v_mov_b32_e32 v140, v18
	v_mov_b32_e32 v141, v18
	v_mov_b32_e32 v142, v18
	v_mov_b32_e32 v143, v18
	v_mov_b32_e32 v144, v18
	v_mov_b32_e32 v145, v18
	v_add_u32_e32 v246, 0x18000, v1
	v_add_u32_e32 v247, 0x1c000, v1
.LBB0_495:
	ds_read_b128 v[2:5], v187
	ds_read_b128 v[6:9], v187 offset:1024
	ds_read_b128 v[10:13], v187 offset:2048
	ds_read_b128 v[14:17], v187 offset:3072
	s_add_u32 s28, s26, 0xfffc0080
	s_addc_u32 s29, s27, -1
	s_cmp_eq_u32 s52, 12
	s_cselect_b32 s31, s6, s29
	s_cselect_b32 s30, s17, s28
	s_cselect_b32 s29, s15, s51
	s_cselect_b32 s28, s49, s50
	s_add_i32 m0, s37, 0xc000
	ds_read_b128 v[192:195], v188
	ds_read_b128 v[196:199], v188 offset:1024
	ds_read_b128 v[206:209], v188 offset:2048
	ds_read_b128 v[210:213], v188 offset:3072
	ds_read_b128 v[214:217], v188 offset:4096
	ds_read_b128 v[218:221], v188 offset:5120
	ds_read_b128 v[222:225], v188 offset:6144
	ds_read_b128 v[226:229], v188 offset:7168
	global_load_lds_dwordx4 v170, s[26:27]
	s_add_i32 m0, s37, 0xe000
	s_nop 0
	global_load_lds_dwordx4 v172, s[26:27]
	s_waitcnt lgkmcnt(8)
	s_barrier
	s_waitcnt lgkmcnt(0)
	s_setprio 1
	s_waitcnt lgkmcnt(0)
	v_mfma_scale_f32_16x16x128_f8f6f4 v[142:145], v[2:9], v[192:199], v[142:145], v189, v189 op_sel_hi:[0,0,0]
	v_mfma_scale_f32_16x16x128_f8f6f4 v[138:141], v[10:17], v[192:199], v[138:141], v189, v189 op_sel_hi:[0,0,0]
	v_mfma_scale_f32_16x16x128_f8f6f4 v[126:129], v[2:9], v[206:213], v[126:129], v189, v189 op_sel_hi:[0,0,0]
	v_mfma_scale_f32_16x16x128_f8f6f4 v[122:125], v[10:17], v[206:213], v[122:125], v189, v189 op_sel_hi:[0,0,0]
	v_mfma_scale_f32_16x16x128_f8f6f4 v[110:113], v[2:9], v[214:221], v[110:113], v189, v189 op_sel_hi:[0,0,0]
	v_mfma_scale_f32_16x16x128_f8f6f4 v[106:109], v[10:17], v[214:221], v[106:109], v189, v189 op_sel_hi:[0,0,0]
	v_mfma_scale_f32_16x16x128_f8f6f4 v[94:97], v[2:9], v[222:229], v[94:97], v189, v189 op_sel_hi:[0,0,0]
	v_mfma_scale_f32_16x16x128_f8f6f4 v[90:93], v[10:17], v[222:229], v[90:93], v189, v189 op_sel_hi:[0,0,0]
	s_setprio 0
	s_barrier
	s_add_i32 s53, s46, s34
	s_mov_b32 m0, s53
	ds_read_b128 v[230:233], v190
	ds_read_b128 v[234:237], v190 offset:1024
	ds_read_b128 v[238:241], v190 offset:2048
	ds_read_b128 v[242:245], v190 offset:3072
	global_load_lds_dwordx4 v150, s[28:29]
	s_add_i32 m0, s53, 0x2000
	s_nop 0
	global_load_lds_dwordx4 v146, s[28:29]
	s_barrier
	s_waitcnt lgkmcnt(0)
	s_setprio 1
	s_waitcnt lgkmcnt(0)
	v_mfma_scale_f32_16x16x128_f8f6f4 v[134:137], v[230:237], v[192:199], v[134:137], v189, v189 op_sel_hi:[0,0,0]
	v_mfma_scale_f32_16x16x128_f8f6f4 v[130:133], v[238:245], v[192:199], v[130:133], v189, v189 op_sel_hi:[0,0,0]
	v_mfma_scale_f32_16x16x128_f8f6f4 v[118:121], v[230:237], v[206:213], v[118:121], v189, v189 op_sel_hi:[0,0,0]
	v_mfma_scale_f32_16x16x128_f8f6f4 v[114:117], v[238:245], v[206:213], v[114:117], v189, v189 op_sel_hi:[0,0,0]
	v_mfma_scale_f32_16x16x128_f8f6f4 v[102:105], v[230:237], v[214:221], v[102:105], v189, v189 op_sel_hi:[0,0,0]
	v_mfma_scale_f32_16x16x128_f8f6f4 v[98:101], v[238:245], v[214:221], v[98:101], v189, v189 op_sel_hi:[0,0,0]
	v_mfma_scale_f32_16x16x128_f8f6f4 v[86:89], v[230:237], v[222:229], v[86:89], v189, v189 op_sel_hi:[0,0,0]
	v_mfma_scale_f32_16x16x128_f8f6f4 v[82:85], v[238:245], v[222:229], v[82:85], v189, v189 op_sel_hi:[0,0,0]
	s_setprio 0
	s_mov_b32 m0, s37
	s_add_u32 s56, s30, 0x80
	s_addc_u32 s57, s31, 0
	s_barrier
	ds_read_b128 v[192:195], v188 offset:16384
	ds_read_b128 v[196:199], v188 offset:17408
	ds_read_b128 v[206:209], v188 offset:18432
	ds_read_b128 v[210:213], v188 offset:19456
	ds_read_b128 v[214:217], v188 offset:20480
	ds_read_b128 v[218:221], v188 offset:21504
	ds_read_b128 v[222:225], v188 offset:22528
	ds_read_b128 v[226:229], v188 offset:23552
	global_load_lds_dwordx4 v152, s[30:31]
	s_mov_b32 m0, s38
	s_nop 0
	global_load_lds_dwordx4 v148, s[30:31]
	s_barrier
	s_waitcnt lgkmcnt(0)
	s_setprio 1
	s_waitcnt lgkmcnt(0)
	v_mfma_scale_f32_16x16x128_f8f6f4 v[78:81], v[2:9], v[192:199], v[78:81], v189, v189 op_sel_hi:[0,0,0]
	v_mfma_scale_f32_16x16x128_f8f6f4 v[74:77], v[10:17], v[192:199], v[74:77], v189, v189 op_sel_hi:[0,0,0]
	v_mfma_scale_f32_16x16x128_f8f6f4 v[62:65], v[2:9], v[206:213], v[62:65], v189, v189 op_sel_hi:[0,0,0]
	v_mfma_scale_f32_16x16x128_f8f6f4 v[58:61], v[10:17], v[206:213], v[58:61], v189, v189 op_sel_hi:[0,0,0]
	v_mfma_scale_f32_16x16x128_f8f6f4 v[46:49], v[2:9], v[214:221], v[46:49], v189, v189 op_sel_hi:[0,0,0]
	v_mfma_scale_f32_16x16x128_f8f6f4 v[42:45], v[10:17], v[214:221], v[42:45], v189, v189 op_sel_hi:[0,0,0]
	v_mfma_scale_f32_16x16x128_f8f6f4 v[30:33], v[2:9], v[222:229], v[30:33], v189, v189 op_sel_hi:[0,0,0]
	v_mfma_scale_f32_16x16x128_f8f6f4 v[26:29], v[10:17], v[222:229], v[26:29], v189, v189 op_sel_hi:[0,0,0]
	s_setprio 0
	s_barrier
	s_add_u32 s54, s28, 0x40000
	s_addc_u32 s55, s29, 0
	s_add_i32 s53, s47, s34
	s_mov_b32 m0, s53
	s_nop 0
	global_load_lds_dwordx4 v150, s[54:55]
	s_add_i32 m0, s53, 0x2000
	s_nop 0
	global_load_lds_dwordx4 v146, s[54:55]
	s_waitcnt vmcnt(6)
	s_barrier
	s_setprio 1
	v_mfma_scale_f32_16x16x128_f8f6f4 v[70:73], v[230:237], v[192:199], v[70:73], v189, v189 op_sel_hi:[0,0,0]
	v_mfma_scale_f32_16x16x128_f8f6f4 v[66:69], v[238:245], v[192:199], v[66:69], v189, v189 op_sel_hi:[0,0,0]
	v_mfma_scale_f32_16x16x128_f8f6f4 v[54:57], v[230:237], v[206:213], v[54:57], v189, v189 op_sel_hi:[0,0,0]
	v_mfma_scale_f32_16x16x128_f8f6f4 v[50:53], v[238:245], v[206:213], v[50:53], v189, v189 op_sel_hi:[0,0,0]
	v_mfma_scale_f32_16x16x128_f8f6f4 v[38:41], v[230:237], v[214:221], v[38:41], v189, v189 op_sel_hi:[0,0,0]
	v_mfma_scale_f32_16x16x128_f8f6f4 v[34:37], v[238:245], v[214:221], v[34:37], v189, v189 op_sel_hi:[0,0,0]
	v_mfma_scale_f32_16x16x128_f8f6f4 v[22:25], v[230:237], v[222:229], v[22:25], v189, v189 op_sel_hi:[0,0,0]
	v_mfma_scale_f32_16x16x128_f8f6f4 v[18:21], v[238:245], v[222:229], v[18:21], v189, v189 op_sel_hi:[0,0,0]
	s_setprio 0
	s_add_i32 s53, 0, 0x18000
	s_barrier
	ds_read_b128 v[2:5], v246
	ds_read_b128 v[6:9], v246 offset:1024
	ds_read_b128 v[10:13], v246 offset:2048
	ds_read_b128 v[14:17], v246 offset:3072
	s_add_u32 s30, s30, 0x40000
	s_addc_u32 s31, s31, 0
	s_mov_b32 m0, s39
	ds_read_b128 v[192:195], v188 offset:32768
	ds_read_b128 v[196:199], v188 offset:33792
	ds_read_b128 v[206:209], v188 offset:34816
	ds_read_b128 v[210:213], v188 offset:35840
	ds_read_b128 v[214:217], v188 offset:36864
	ds_read_b128 v[218:221], v188 offset:37888
	ds_read_b128 v[222:225], v188 offset:38912
	ds_read_b128 v[226:229], v188 offset:39936
	global_load_lds_dwordx4 v152, s[30:31]
	s_mov_b32 m0, s40
	s_nop 0
	global_load_lds_dwordx4 v148, s[30:31]
	s_waitcnt lgkmcnt(8)
	s_barrier
	s_waitcnt lgkmcnt(0)
	s_setprio 1
	s_waitcnt lgkmcnt(0)
	v_mfma_scale_f32_16x16x128_f8f6f4 v[142:145], v[2:9], v[192:199], v[142:145], v189, v189 op_sel_hi:[0,0,0]
	v_mfma_scale_f32_16x16x128_f8f6f4 v[138:141], v[10:17], v[192:199], v[138:141], v189, v189 op_sel_hi:[0,0,0]
	v_mfma_scale_f32_16x16x128_f8f6f4 v[126:129], v[2:9], v[206:213], v[126:129], v189, v189 op_sel_hi:[0,0,0]
	v_mfma_scale_f32_16x16x128_f8f6f4 v[122:125], v[10:17], v[206:213], v[122:125], v189, v189 op_sel_hi:[0,0,0]
	v_mfma_scale_f32_16x16x128_f8f6f4 v[110:113], v[2:9], v[214:221], v[110:113], v189, v189 op_sel_hi:[0,0,0]
	v_mfma_scale_f32_16x16x128_f8f6f4 v[106:109], v[10:17], v[214:221], v[106:109], v189, v189 op_sel_hi:[0,0,0]
	v_mfma_scale_f32_16x16x128_f8f6f4 v[94:97], v[2:9], v[222:229], v[94:97], v189, v189 op_sel_hi:[0,0,0]
	v_mfma_scale_f32_16x16x128_f8f6f4 v[90:93], v[10:17], v[222:229], v[90:93], v189, v189 op_sel_hi:[0,0,0]
	s_setprio 0
	s_barrier
	s_add_i32 s30, 0, 0x1c000
	s_add_i32 s31, s53, s34
	s_add_u32 s54, s28, 0x80
	s_addc_u32 s55, s29, 0
	s_mov_b32 m0, s31
	ds_read_b128 v[230:233], v247
	ds_read_b128 v[234:237], v247 offset:1024
	ds_read_b128 v[238:241], v247 offset:2048
	ds_read_b128 v[242:245], v247 offset:3072
	global_load_lds_dwordx4 v150, s[54:55]
	s_add_i32 m0, s31, 0x2000
	s_nop 0
	global_load_lds_dwordx4 v146, s[54:55]
	s_barrier
	s_waitcnt lgkmcnt(0)
	s_setprio 1
	s_waitcnt lgkmcnt(0)
	v_mfma_scale_f32_16x16x128_f8f6f4 v[134:137], v[230:237], v[192:199], v[134:137], v189, v189 op_sel_hi:[0,0,0]
	v_mfma_scale_f32_16x16x128_f8f6f4 v[130:133], v[238:245], v[192:199], v[130:133], v189, v189 op_sel_hi:[0,0,0]
	v_mfma_scale_f32_16x16x128_f8f6f4 v[118:121], v[230:237], v[206:213], v[118:121], v189, v189 op_sel_hi:[0,0,0]
	v_mfma_scale_f32_16x16x128_f8f6f4 v[114:117], v[238:245], v[206:213], v[114:117], v189, v189 op_sel_hi:[0,0,0]
	v_mfma_scale_f32_16x16x128_f8f6f4 v[102:105], v[230:237], v[214:221], v[102:105], v189, v189 op_sel_hi:[0,0,0]
	v_mfma_scale_f32_16x16x128_f8f6f4 v[98:101], v[238:245], v[214:221], v[98:101], v189, v189 op_sel_hi:[0,0,0]
	v_mfma_scale_f32_16x16x128_f8f6f4 v[86:89], v[230:237], v[222:229], v[86:89], v189, v189 op_sel_hi:[0,0,0]
	v_mfma_scale_f32_16x16x128_f8f6f4 v[82:85], v[238:245], v[222:229], v[82:85], v189, v189 op_sel_hi:[0,0,0]
	s_setprio 0
	s_mov_b32 m0, s43
	s_barrier
	ds_read_b128 v[192:195], v188 offset:49152
	ds_read_b128 v[196:199], v188 offset:50176
	ds_read_b128 v[206:209], v188 offset:51200
	ds_read_b128 v[210:213], v188 offset:52224
	ds_read_b128 v[214:217], v188 offset:53248
	ds_read_b128 v[218:221], v188 offset:54272
	ds_read_b128 v[222:225], v188 offset:55296
	ds_read_b128 v[226:229], v188 offset:56320
	global_load_lds_dwordx4 v152, s[56:57]
	s_mov_b32 m0, s44
	s_nop 0
	global_load_lds_dwordx4 v148, s[56:57]
	s_barrier
	s_waitcnt lgkmcnt(0)
	s_setprio 1
	s_waitcnt lgkmcnt(0)
	v_mfma_scale_f32_16x16x128_f8f6f4 v[78:81], v[2:9], v[192:199], v[78:81], v189, v189 op_sel_hi:[0,0,0]
	v_mfma_scale_f32_16x16x128_f8f6f4 v[74:77], v[10:17], v[192:199], v[74:77], v189, v189 op_sel_hi:[0,0,0]
	v_mfma_scale_f32_16x16x128_f8f6f4 v[62:65], v[2:9], v[206:213], v[62:65], v189, v189 op_sel_hi:[0,0,0]
	v_mfma_scale_f32_16x16x128_f8f6f4 v[58:61], v[10:17], v[206:213], v[58:61], v189, v189 op_sel_hi:[0,0,0]
	v_mfma_scale_f32_16x16x128_f8f6f4 v[46:49], v[2:9], v[214:221], v[46:49], v189, v189 op_sel_hi:[0,0,0]
	v_mfma_scale_f32_16x16x128_f8f6f4 v[42:45], v[10:17], v[214:221], v[42:45], v189, v189 op_sel_hi:[0,0,0]
	v_mfma_scale_f32_16x16x128_f8f6f4 v[30:33], v[2:9], v[222:229], v[30:33], v189, v189 op_sel_hi:[0,0,0]
	v_mfma_scale_f32_16x16x128_f8f6f4 v[26:29], v[10:17], v[222:229], v[26:29], v189, v189 op_sel_hi:[0,0,0]
	s_setprio 0
	s_barrier
	s_add_u32 s28, s28, 0x40080
	s_addc_u32 s29, s29, 0
	s_add_i32 s30, s30, s34
	s_mov_b32 m0, s30
	s_nop 0
	global_load_lds_dwordx4 v150, s[28:29]
	s_add_i32 m0, s30, 0x2000
	s_nop 0
	global_load_lds_dwordx4 v146, s[28:29]
	s_waitcnt vmcnt(6)
	s_barrier
	s_setprio 1
	v_mfma_scale_f32_16x16x128_f8f6f4 v[70:73], v[230:237], v[192:199], v[70:73], v189, v189 op_sel_hi:[0,0,0]
	v_mfma_scale_f32_16x16x128_f8f6f4 v[66:69], v[238:245], v[192:199], v[66:69], v189, v189 op_sel_hi:[0,0,0]
	v_mfma_scale_f32_16x16x128_f8f6f4 v[54:57], v[230:237], v[206:213], v[54:57], v189, v189 op_sel_hi:[0,0,0]
	v_mfma_scale_f32_16x16x128_f8f6f4 v[50:53], v[238:245], v[206:213], v[50:53], v189, v189 op_sel_hi:[0,0,0]
	v_mfma_scale_f32_16x16x128_f8f6f4 v[38:41], v[230:237], v[214:221], v[38:41], v189, v189 op_sel_hi:[0,0,0]
	v_mfma_scale_f32_16x16x128_f8f6f4 v[34:37], v[238:245], v[214:221], v[34:37], v189, v189 op_sel_hi:[0,0,0]
	v_mfma_scale_f32_16x16x128_f8f6f4 v[22:25], v[230:237], v[222:229], v[22:25], v189, v189 op_sel_hi:[0,0,0]
	v_mfma_scale_f32_16x16x128_f8f6f4 v[18:21], v[238:245], v[222:229], v[18:21], v189, v189 op_sel_hi:[0,0,0]
	s_setprio 0
	s_add_i32 s52, s52, 2
	s_add_u32 s26, s26, 0x100
	s_addc_u32 s27, s27, 0
	s_add_u32 s50, s50, 0x100
	s_addc_u32 s51, s51, 0
	s_cmp_gt_u32 s52, 13
	s_barrier
	s_cbranch_scc0 .LBB0_495
	s_lshl_b32 s28, s22, 8
	s_cmpk_gt_i32 s22, 0x7f
	s_mov_b64 s[30:31], -1
	s_cbranch_scc0 .LBB0_498
	s_add_i32 s6, s28, 0xffff8000
	v_readlane_b32 s60, v254, 18
	s_lshl_b64 s[26:27], s[6:7], 13
	v_readlane_b32 s64, v254, 22
	v_readlane_b32 s65, v254, 23
	s_add_u32 s26, s64, s26
	v_readlane_b32 s61, v254, 19
	v_readlane_b32 s62, v254, 20
	v_readlane_b32 s63, v254, 21
	v_readlane_b32 s66, v254, 24
	v_readlane_b32 s67, v254, 25
	v_readlane_b32 s68, v254, 26
	v_readlane_b32 s69, v254, 27
	v_readlane_b32 s70, v254, 28
	v_readlane_b32 s71, v254, 29
	v_readlane_b32 s72, v254, 30
	v_readlane_b32 s73, v254, 31
	v_readlane_b32 s74, v254, 32
	v_readlane_b32 s75, v254, 33
	s_addc_u32 s27, s65, s27
	s_mov_b32 s29, s7
	s_mov_b64 s[30:31], 0

.LBB0_819:
	s_ashr_i32 s17, s16, 31
	v_cmp_lt_i64_e32 vcc, s[18:19], v[162:163]
	s_lshl_b64 s[18:19], s[16:17], 19
	s_add_u32 s18, s3, s18
	s_addc_u32 s19, s9, s19
	s_and_b64 s[20:21], vcc, exec
	s_cselect_b32 s17, s19, s25
	s_cselect_b32 s23, s18, s24
	s_ashr_i32 s15, s14, 31
	s_lshl_b64 s[20:21], s[14:15], 19
	s_add_u32 s20, s30, s20
	s_addc_u32 s21, s31, s21
	s_and_b64 s[28:29], vcc, exec
	s_cselect_b32 s15, s21, s27
	s_cselect_b32 s56, s20, s26
	s_add_u32 s24, s24, 0x40080
	s_addc_u32 s25, s25, 0
	s_add_u32 s57, s26, 0x100
	v_mov_b32_e32 v18, 0
	s_addc_u32 s59, s27, 0
	s_mov_b32 s60, -2
	v_mov_b32_e32 v19, v18
	v_mov_b32_e32 v20, v18
	v_mov_b32_e32 v21, v18
	v_mov_b32_e32 v22, v18
	v_mov_b32_e32 v23, v18
	v_mov_b32_e32 v24, v18
	v_mov_b32_e32 v25, v18
	v_mov_b32_e32 v30, v18
	v_mov_b32_e32 v31, v18
	v_mov_b32_e32 v32, v18
	v_mov_b32_e32 v33, v18
	v_mov_b32_e32 v38, v18
	v_mov_b32_e32 v39, v18
	v_mov_b32_e32 v40, v18
	v_mov_b32_e32 v41, v18
	v_mov_b32_e32 v46, v18
	v_mov_b32_e32 v47, v18
	v_mov_b32_e32 v48, v18
	v_mov_b32_e32 v49, v18
	v_mov_b32_e32 v54, v18
	v_mov_b32_e32 v55, v18
	v_mov_b32_e32 v56, v18
	v_mov_b32_e32 v57, v18
	v_mov_b32_e32 v66, v18
	v_mov_b32_e32 v67, v18
	v_mov_b32_e32 v68, v18
	v_mov_b32_e32 v69, v18
	v_mov_b32_e32 v70, v18
	v_mov_b32_e32 v71, v18
	v_mov_b32_e32 v72, v18
	v_mov_b32_e32 v73, v18
	v_mov_b32_e32 v26, v18
	v_mov_b32_e32 v27, v18
	v_mov_b32_e32 v28, v18
	v_mov_b32_e32 v29, v18
	v_mov_b32_e32 v34, v18
	v_mov_b32_e32 v35, v18
	v_mov_b32_e32 v36, v18
	v_mov_b32_e32 v37, v18
	v_mov_b32_e32 v42, v18
	v_mov_b32_e32 v43, v18
	v_mov_b32_e32 v44, v18
	v_mov_b32_e32 v45, v18
	v_mov_b32_e32 v50, v18
	v_mov_b32_e32 v51, v18
	v_mov_b32_e32 v52, v18
	v_mov_b32_e32 v53, v18
	v_mov_b32_e32 v58, v18
	v_mov_b32_e32 v59, v18
	v_mov_b32_e32 v60, v18
	v_mov_b32_e32 v61, v18
	v_mov_b32_e32 v62, v18
	v_mov_b32_e32 v63, v18
	v_mov_b32_e32 v64, v18
	v_mov_b32_e32 v65, v18
	v_mov_b32_e32 v74, v18
	v_mov_b32_e32 v75, v18
	v_mov_b32_e32 v76, v18
	v_mov_b32_e32 v77, v18
	v_mov_b32_e32 v78, v18
	v_mov_b32_e32 v79, v18
	v_mov_b32_e32 v80, v18
	v_mov_b32_e32 v81, v18
	v_mov_b32_e32 v82, v18
	v_mov_b32_e32 v83, v18
	v_mov_b32_e32 v84, v18
	v_mov_b32_e32 v85, v18
	v_mov_b32_e32 v86, v18
	v_mov_b32_e32 v87, v18
	v_mov_b32_e32 v88, v18
	v_mov_b32_e32 v89, v18
	v_mov_b32_e32 v98, v18
	v_mov_b32_e32 v99, v18
	v_mov_b32_e32 v100, v18
	v_mov_b32_e32 v101, v18
	v_mov_b32_e32 v102, v18
	v_mov_b32_e32 v103, v18
	v_mov_b32_e32 v104, v18
	v_mov_b32_e32 v105, v18
	v_mov_b32_e32 v114, v18
	v_mov_b32_e32 v115, v18
	v_mov_b32_e32 v116, v18
	v_mov_b32_e32 v117, v18
	v_mov_b32_e32 v118, v18
	v_mov_b32_e32 v119, v18
	v_mov_b32_e32 v120, v18
	v_mov_b32_e32 v121, v18
	v_mov_b32_e32 v130, v18
	v_mov_b32_e32 v131, v18
	v_mov_b32_e32 v132, v18
	v_mov_b32_e32 v133, v18
	v_mov_b32_e32 v134, v18
	v_mov_b32_e32 v135, v18
	v_mov_b32_e32 v136, v18
	v_mov_b32_e32 v137, v18
	v_mov_b32_e32 v90, v18
	v_mov_b32_e32 v91, v18
	v_mov_b32_e32 v92, v18
	v_mov_b32_e32 v93, v18
	v_mov_b32_e32 v94, v18
	v_mov_b32_e32 v95, v18
	v_mov_b32_e32 v96, v18
	v_mov_b32_e32 v97, v18
	v_mov_b32_e32 v106, v18
	v_mov_b32_e32 v107, v18
	v_mov_b32_e32 v108, v18
	v_mov_b32_e32 v109, v18
	v_mov_b32_e32 v110, v18
	v_mov_b32_e32 v111, v18
	v_mov_b32_e32 v112, v18
	v_mov_b32_e32 v113, v18
	v_mov_b32_e32 v122, v18
	v_mov_b32_e32 v123, v18
	v_mov_b32_e32 v124, v18
	v_mov_b32_e32 v125, v18
	v_mov_b32_e32 v126, v18
	v_mov_b32_e32 v127, v18
	v_mov_b32_e32 v128, v18
	v_mov_b32_e32 v129, v18
	v_mov_b32_e32 v138, v18
	v_mov_b32_e32 v139, v18
	v_mov_b32_e32 v140, v18
	v_mov_b32_e32 v141, v18
	v_mov_b32_e32 v142, v18
	v_mov_b32_e32 v143, v18
	v_mov_b32_e32 v144, v18
	v_mov_b32_e32 v145, v18
	v_add_u32_e32 v172, 0x18000, v175
	v_add_u32_e32 v173, 0x1c000, v175
.LBB0_820:
	ds_read_b128 v[2:5], v176
	ds_read_b128 v[6:9], v176 offset:1024
	ds_read_b128 v[10:13], v176 offset:2048
	ds_read_b128 v[14:17], v176 offset:3072
	s_add_u32 s26, s24, 0xfffc0080
	s_addc_u32 s27, s25, -1
	s_cmp_eq_u32 s60, 12
	s_cselect_b32 s29, s17, s27
	s_cselect_b32 s28, s23, s26
	s_cselect_b32 s27, s15, s59
	s_cselect_b32 s26, s56, s57
	s_add_i32 m0, s36, 0xc000
	ds_read_b128 v[190:193], v177
	ds_read_b128 v[194:197], v177 offset:1024
	ds_read_b128 v[214:217], v177 offset:2048
	ds_read_b128 v[218:221], v177 offset:3072
	ds_read_b128 v[222:225], v177 offset:4096
	ds_read_b128 v[226:229], v177 offset:5120
	ds_read_b128 v[230:233], v177 offset:6144
	ds_read_b128 v[234:237], v177 offset:7168
	global_load_lds_dwordx4 v158, s[24:25]
	s_add_i32 m0, s36, 0xe000
	s_nop 0
	global_load_lds_dwordx4 v160, s[24:25]
	s_waitcnt lgkmcnt(8)
	s_barrier
	s_waitcnt lgkmcnt(0)
	s_setprio 1
	s_waitcnt lgkmcnt(0)
	v_mfma_scale_f32_16x16x128_f8f6f4 v[142:145], v[2:9], v[190:197], v[142:145], v178, v178 op_sel_hi:[0,0,0]
	v_mfma_scale_f32_16x16x128_f8f6f4 v[138:141], v[10:17], v[190:197], v[138:141], v178, v178 op_sel_hi:[0,0,0]
	v_mfma_scale_f32_16x16x128_f8f6f4 v[126:129], v[2:9], v[214:221], v[126:129], v178, v178 op_sel_hi:[0,0,0]
	v_mfma_scale_f32_16x16x128_f8f6f4 v[122:125], v[10:17], v[214:221], v[122:125], v178, v178 op_sel_hi:[0,0,0]
	v_mfma_scale_f32_16x16x128_f8f6f4 v[110:113], v[2:9], v[222:229], v[110:113], v178, v178 op_sel_hi:[0,0,0]
	v_mfma_scale_f32_16x16x128_f8f6f4 v[106:109], v[10:17], v[222:229], v[106:109], v178, v178 op_sel_hi:[0,0,0]
	v_mfma_scale_f32_16x16x128_f8f6f4 v[94:97], v[2:9], v[230:237], v[94:97], v178, v178 op_sel_hi:[0,0,0]
	v_mfma_scale_f32_16x16x128_f8f6f4 v[90:93], v[10:17], v[230:237], v[90:93], v178, v178 op_sel_hi:[0,0,0]
	s_setprio 0
	s_barrier
	s_add_i32 s61, s48, s33
	s_add_u32 s66, s26, 0x80
	s_addc_u32 s67, s27, 0
	s_mov_b32 m0, s61
	ds_read_b128 v[238:241], v179
	ds_read_b128 v[242:245], v179 offset:1024
	ds_read_b128 v[246:249], v179 offset:2048
	ds_read_b128 v[250:253], v179 offset:3072
	global_load_lds_dwordx4 v150, s[26:27]
	s_add_i32 m0, s61, 0x2000
	s_nop 0
	global_load_lds_dwordx4 v146, s[26:27]
	s_barrier
	s_waitcnt lgkmcnt(0)
	s_setprio 1
	s_waitcnt lgkmcnt(0)
	v_mfma_scale_f32_16x16x128_f8f6f4 v[134:137], v[238:245], v[190:197], v[134:137], v178, v178 op_sel_hi:[0,0,0]
	v_mfma_scale_f32_16x16x128_f8f6f4 v[130:133], v[246:253], v[190:197], v[130:133], v178, v178 op_sel_hi:[0,0,0]
	v_mfma_scale_f32_16x16x128_f8f6f4 v[118:121], v[238:245], v[214:221], v[118:121], v178, v178 op_sel_hi:[0,0,0]
	v_mfma_scale_f32_16x16x128_f8f6f4 v[114:117], v[246:253], v[214:221], v[114:117], v178, v178 op_sel_hi:[0,0,0]
	v_mfma_scale_f32_16x16x128_f8f6f4 v[102:105], v[238:245], v[222:229], v[102:105], v178, v178 op_sel_hi:[0,0,0]
	v_mfma_scale_f32_16x16x128_f8f6f4 v[98:101], v[246:253], v[222:229], v[98:101], v178, v178 op_sel_hi:[0,0,0]
	v_mfma_scale_f32_16x16x128_f8f6f4 v[86:89], v[238:245], v[230:237], v[86:89], v178, v178 op_sel_hi:[0,0,0]
	v_mfma_scale_f32_16x16x128_f8f6f4 v[82:85], v[246:253], v[230:237], v[82:85], v178, v178 op_sel_hi:[0,0,0]
	s_setprio 0
	s_mov_b32 m0, s36
	s_add_u32 s68, s28, 0x80
	s_addc_u32 s69, s29, 0
	s_barrier
	ds_read_b128 v[190:193], v177 offset:16384
	ds_read_b128 v[194:197], v177 offset:17408
	ds_read_b128 v[214:217], v177 offset:18432
	ds_read_b128 v[218:221], v177 offset:19456
	ds_read_b128 v[222:225], v177 offset:20480
	ds_read_b128 v[226:229], v177 offset:21504
	ds_read_b128 v[230:233], v177 offset:22528
	ds_read_b128 v[234:237], v177 offset:23552
	global_load_lds_dwordx4 v152, s[28:29]
	s_mov_b32 m0, s37
	s_nop 0
	global_load_lds_dwordx4 v148, s[28:29]
	s_barrier
	s_waitcnt lgkmcnt(0)
	s_setprio 1
	s_waitcnt lgkmcnt(0)
	v_mfma_scale_f32_16x16x128_f8f6f4 v[78:81], v[2:9], v[190:197], v[78:81], v178, v178 op_sel_hi:[0,0,0]
	v_mfma_scale_f32_16x16x128_f8f6f4 v[74:77], v[10:17], v[190:197], v[74:77], v178, v178 op_sel_hi:[0,0,0]
	v_mfma_scale_f32_16x16x128_f8f6f4 v[62:65], v[2:9], v[214:221], v[62:65], v178, v178 op_sel_hi:[0,0,0]
	v_mfma_scale_f32_16x16x128_f8f6f4 v[58:61], v[10:17], v[214:221], v[58:61], v178, v178 op_sel_hi:[0,0,0]
	v_mfma_scale_f32_16x16x128_f8f6f4 v[50:53], v[2:9], v[222:229], v[50:53], v178, v178 op_sel_hi:[0,0,0]
	v_mfma_scale_f32_16x16x128_f8f6f4 v[42:45], v[10:17], v[222:229], v[42:45], v178, v178 op_sel_hi:[0,0,0]
	v_mfma_scale_f32_16x16x128_f8f6f4 v[34:37], v[2:9], v[230:237], v[34:37], v178, v178 op_sel_hi:[0,0,0]
	v_mfma_scale_f32_16x16x128_f8f6f4 v[26:29], v[10:17], v[230:237], v[26:29], v178, v178 op_sel_hi:[0,0,0]
	s_setprio 0
	s_barrier
	s_add_u32 s62, s26, 0x40000
	s_addc_u32 s63, s27, 0
	s_add_i32 s61, s49, s33
	s_mov_b32 m0, s61
	s_nop 0
	global_load_lds_dwordx4 v150, s[62:63]
	s_add_i32 m0, s61, 0x2000
	s_nop 0
	global_load_lds_dwordx4 v146, s[62:63]
	s_waitcnt vmcnt(6)
	s_barrier
	s_setprio 1
	v_mfma_scale_f32_16x16x128_f8f6f4 v[70:73], v[238:245], v[190:197], v[70:73], v178, v178 op_sel_hi:[0,0,0]
	v_mfma_scale_f32_16x16x128_f8f6f4 v[66:69], v[246:253], v[190:197], v[66:69], v178, v178 op_sel_hi:[0,0,0]
	v_mfma_scale_f32_16x16x128_f8f6f4 v[54:57], v[238:245], v[214:221], v[54:57], v178, v178 op_sel_hi:[0,0,0]
	v_mfma_scale_f32_16x16x128_f8f6f4 v[46:49], v[246:253], v[214:221], v[46:49], v178, v178 op_sel_hi:[0,0,0]
	v_mfma_scale_f32_16x16x128_f8f6f4 v[38:41], v[238:245], v[222:229], v[38:41], v178, v178 op_sel_hi:[0,0,0]
	v_mfma_scale_f32_16x16x128_f8f6f4 v[30:33], v[246:253], v[222:229], v[30:33], v178, v178 op_sel_hi:[0,0,0]
	v_mfma_scale_f32_16x16x128_f8f6f4 v[22:25], v[238:245], v[230:237], v[22:25], v178, v178 op_sel_hi:[0,0,0]
	v_mfma_scale_f32_16x16x128_f8f6f4 v[18:21], v[246:253], v[230:237], v[18:21], v178, v178 op_sel_hi:[0,0,0]
	s_setprio 0
	s_add_i32 s61, 0, 0x18000
	s_barrier
	ds_read_b128 v[2:5], v172
	ds_read_b128 v[6:9], v172 offset:1024
	ds_read_b128 v[10:13], v172 offset:2048
	ds_read_b128 v[14:17], v172 offset:3072
	s_add_u32 s28, s28, 0x40000
	s_addc_u32 s29, s29, 0
	s_mov_b32 m0, s38
	ds_read_b128 v[190:193], v177 offset:32768
	ds_read_b128 v[194:197], v177 offset:33792
	ds_read_b128 v[214:217], v177 offset:34816
	ds_read_b128 v[218:221], v177 offset:35840
	ds_read_b128 v[222:225], v177 offset:36864
	ds_read_b128 v[226:229], v177 offset:37888
	ds_read_b128 v[230:233], v177 offset:38912
	ds_read_b128 v[234:237], v177 offset:39936
	global_load_lds_dwordx4 v152, s[28:29]
	s_mov_b32 m0, s39
	s_nop 0
	global_load_lds_dwordx4 v148, s[28:29]
	s_waitcnt lgkmcnt(8)
	s_barrier
	s_waitcnt lgkmcnt(0)
	s_setprio 1
	s_waitcnt lgkmcnt(0)
	v_mfma_scale_f32_16x16x128_f8f6f4 v[142:145], v[2:9], v[190:197], v[142:145], v178, v178 op_sel_hi:[0,0,0]
	v_mfma_scale_f32_16x16x128_f8f6f4 v[138:141], v[10:17], v[190:197], v[138:141], v178, v178 op_sel_hi:[0,0,0]
	v_mfma_scale_f32_16x16x128_f8f6f4 v[126:129], v[2:9], v[214:221], v[126:129], v178, v178 op_sel_hi:[0,0,0]
	v_mfma_scale_f32_16x16x128_f8f6f4 v[122:125], v[10:17], v[214:221], v[122:125], v178, v178 op_sel_hi:[0,0,0]
	v_mfma_scale_f32_16x16x128_f8f6f4 v[110:113], v[2:9], v[222:229], v[110:113], v178, v178 op_sel_hi:[0,0,0]
	v_mfma_scale_f32_16x16x128_f8f6f4 v[106:109], v[10:17], v[222:229], v[106:109], v178, v178 op_sel_hi:[0,0,0]
	v_mfma_scale_f32_16x16x128_f8f6f4 v[94:97], v[2:9], v[230:237], v[94:97], v178, v178 op_sel_hi:[0,0,0]
	v_mfma_scale_f32_16x16x128_f8f6f4 v[90:93], v[10:17], v[230:237], v[90:93], v178, v178 op_sel_hi:[0,0,0]
	s_setprio 0
	s_barrier
	s_add_i32 s28, 0, 0x1c000
	s_add_i32 s29, s61, s33
	s_mov_b32 m0, s29
	ds_read_b128 v[238:241], v173
	ds_read_b128 v[242:245], v173 offset:1024
	ds_read_b128 v[246:249], v173 offset:2048
	ds_read_b128 v[250:253], v173 offset:3072
	global_load_lds_dwordx4 v150, s[66:67]
	s_add_i32 m0, s29, 0x2000
	s_nop 0
	global_load_lds_dwordx4 v146, s[66:67]
	s_barrier
	s_waitcnt lgkmcnt(0)
	s_setprio 1
	s_waitcnt lgkmcnt(0)
	v_mfma_scale_f32_16x16x128_f8f6f4 v[134:137], v[238:245], v[190:197], v[134:137], v178, v178 op_sel_hi:[0,0,0]
	v_mfma_scale_f32_16x16x128_f8f6f4 v[130:133], v[246:253], v[190:197], v[130:133], v178, v178 op_sel_hi:[0,0,0]
	v_mfma_scale_f32_16x16x128_f8f6f4 v[118:121], v[238:245], v[214:221], v[118:121], v178, v178 op_sel_hi:[0,0,0]
	v_mfma_scale_f32_16x16x128_f8f6f4 v[114:117], v[246:253], v[214:221], v[114:117], v178, v178 op_sel_hi:[0,0,0]
	v_mfma_scale_f32_16x16x128_f8f6f4 v[102:105], v[238:245], v[222:229], v[102:105], v178, v178 op_sel_hi:[0,0,0]
	v_mfma_scale_f32_16x16x128_f8f6f4 v[98:101], v[246:253], v[222:229], v[98:101], v178, v178 op_sel_hi:[0,0,0]
	v_mfma_scale_f32_16x16x128_f8f6f4 v[86:89], v[238:245], v[230:237], v[86:89], v178, v178 op_sel_hi:[0,0,0]
	v_mfma_scale_f32_16x16x128_f8f6f4 v[82:85], v[246:253], v[230:237], v[82:85], v178, v178 op_sel_hi:[0,0,0]
	s_setprio 0
	s_mov_b32 m0, s45
	s_barrier
	ds_read_b128 v[190:193], v177 offset:49152
	ds_read_b128 v[194:197], v177 offset:50176
	ds_read_b128 v[214:217], v177 offset:51200
	ds_read_b128 v[218:221], v177 offset:52224
	ds_read_b128 v[222:225], v177 offset:53248
	ds_read_b128 v[226:229], v177 offset:54272
	ds_read_b128 v[230:233], v177 offset:55296
	ds_read_b128 v[234:237], v177 offset:56320
	global_load_lds_dwordx4 v152, s[68:69]
	s_mov_b32 m0, s46
	s_nop 0
	global_load_lds_dwordx4 v148, s[68:69]
	s_barrier
	s_waitcnt lgkmcnt(0)
	s_setprio 1
	s_waitcnt lgkmcnt(0)
	v_mfma_scale_f32_16x16x128_f8f6f4 v[78:81], v[2:9], v[190:197], v[78:81], v178, v178 op_sel_hi:[0,0,0]
	v_mfma_scale_f32_16x16x128_f8f6f4 v[74:77], v[10:17], v[190:197], v[74:77], v178, v178 op_sel_hi:[0,0,0]
	v_mfma_scale_f32_16x16x128_f8f6f4 v[62:65], v[2:9], v[214:221], v[62:65], v178, v178 op_sel_hi:[0,0,0]
	v_mfma_scale_f32_16x16x128_f8f6f4 v[58:61], v[10:17], v[214:221], v[58:61], v178, v178 op_sel_hi:[0,0,0]
	v_mfma_scale_f32_16x16x128_f8f6f4 v[50:53], v[2:9], v[222:229], v[50:53], v178, v178 op_sel_hi:[0,0,0]
	v_mfma_scale_f32_16x16x128_f8f6f4 v[42:45], v[10:17], v[222:229], v[42:45], v178, v178 op_sel_hi:[0,0,0]
	v_mfma_scale_f32_16x16x128_f8f6f4 v[34:37], v[2:9], v[230:237], v[34:37], v178, v178 op_sel_hi:[0,0,0]
	v_mfma_scale_f32_16x16x128_f8f6f4 v[26:29], v[10:17], v[230:237], v[26:29], v178, v178 op_sel_hi:[0,0,0]
	s_setprio 0
	s_barrier
	s_add_u32 s26, s26, 0x40080
	s_addc_u32 s27, s27, 0
	s_add_i32 s28, s28, s33
	s_mov_b32 m0, s28
	s_nop 0
	global_load_lds_dwordx4 v150, s[26:27]
	s_add_i32 m0, s28, 0x2000
	s_nop 0
	global_load_lds_dwordx4 v146, s[26:27]
	s_waitcnt vmcnt(6)
	s_barrier
	s_setprio 1
	v_mfma_scale_f32_16x16x128_f8f6f4 v[70:73], v[238:245], v[190:197], v[70:73], v178, v178 op_sel_hi:[0,0,0]
	v_mfma_scale_f32_16x16x128_f8f6f4 v[66:69], v[246:253], v[190:197], v[66:69], v178, v178 op_sel_hi:[0,0,0]
	v_mfma_scale_f32_16x16x128_f8f6f4 v[54:57], v[238:245], v[214:221], v[54:57], v178, v178 op_sel_hi:[0,0,0]
	v_mfma_scale_f32_16x16x128_f8f6f4 v[46:49], v[246:253], v[214:221], v[46:49], v178, v178 op_sel_hi:[0,0,0]
	v_mfma_scale_f32_16x16x128_f8f6f4 v[38:41], v[238:245], v[222:229], v[38:41], v178, v178 op_sel_hi:[0,0,0]
	v_mfma_scale_f32_16x16x128_f8f6f4 v[30:33], v[246:253], v[222:229], v[30:33], v178, v178 op_sel_hi:[0,0,0]
	v_mfma_scale_f32_16x16x128_f8f6f4 v[22:25], v[238:245], v[230:237], v[22:25], v178, v178 op_sel_hi:[0,0,0]
	v_mfma_scale_f32_16x16x128_f8f6f4 v[18:21], v[246:253], v[230:237], v[18:21], v178, v178 op_sel_hi:[0,0,0]
	s_setprio 0
	s_add_i32 s60, s60, 2
	s_add_u32 s24, s24, 0x100
	s_addc_u32 s25, s25, 0
	s_add_u32 s57, s57, 0x100
	s_addc_u32 s59, s59, 0
	s_cmp_gt_u32 s60, 13
	s_barrier
	s_cbranch_scc0 .LBB0_820
	v_lshl_add_u32 v10, s22, 8, v174
	s_add_i32 s15, s55, -4
	s_mov_b64 s[22:23], -1
	s_cmp_lt_u32 s15, 8
	v_or_b32_e32 v8, 16, v10
	v_or_b32_e32 v4, 32, v10
	v_or_b32_e32 v2, 48, v10
	s_cbranch_scc1 .LBB0_823
	s_lshl_b32 s22, s55, 8
	s_ashr_i32 s23, s22, 31
	v_mov_b64_e32 v[6:7], s[96:97]
	v_mad_i64_i32 v[12:13], s[24:25], v10, s50, v[6:7]
	s_lshl_b64 s[22:23], s[22:23], 1
	v_lshl_add_u64 v[12:13], v[12:13], 0, s[22:23]
	v_lshlrev_b32_e32 v154, 1, v156
	v_lshl_add_u64 v[16:17], v[12:13], 0, v[154:155]
	v_pk_mul_f32 v[14:15], v[144:145], s[8:9] op_sel_hi:[1,0]
	v_pk_mul_f32 v[12:13], v[142:143], s[8:9] op_sel_hi:[1,0]
	v_pk_mul_f32 v[166:167], v[140:141], s[8:9] op_sel_hi:[1,0]
	v_pk_mul_f32 v[168:169], v[138:139], s[8:9] op_sel_hi:[1,0]
	v_cvt_pk_bf16_f32 v12, v12, v13
	v_cvt_pk_bf16_f32 v13, v14, v15
	v_cvt_pk_bf16_f32 v14, v168, v169
	v_cvt_pk_bf16_f32 v15, v166, v167
	global_store_dwordx4 v[16:17], v[12:15], off
	v_pk_mul_f32 v[166:167], v[132:133], s[8:9] op_sel_hi:[1,0]
	v_pk_mul_f32 v[168:169], v[130:131], s[8:9] op_sel_hi:[1,0]
	v_pk_mul_f32 v[14:15], v[136:137], s[8:9] op_sel_hi:[1,0]
	v_pk_mul_f32 v[12:13], v[134:135], s[8:9] op_sel_hi:[1,0]
	v_add_u32_e32 v3, 0x80, v10
	v_cvt_pk_bf16_f32 v12, v12, v13
	v_cvt_pk_bf16_f32 v13, v14, v15
	v_cvt_pk_bf16_f32 v14, v168, v169
	v_cvt_pk_bf16_f32 v15, v166, v167
	global_store_dwordx4 v[16:17], v[12:15], off offset:256
	v_pk_mul_f32 v[166:167], v[124:125], s[8:9] op_sel_hi:[1,0]
	v_pk_mul_f32 v[168:169], v[122:123], s[8:9] op_sel_hi:[1,0]
	v_mad_i64_i32 v[12:13], s[24:25], v8, s50, v[6:7]
	v_lshl_add_u64 v[12:13], v[12:13], 0, s[22:23]
	v_lshl_add_u64 v[16:17], v[12:13], 0, v[154:155]
	v_pk_mul_f32 v[14:15], v[128:129], s[8:9] op_sel_hi:[1,0]
	v_pk_mul_f32 v[12:13], v[126:127], s[8:9] op_sel_hi:[1,0]
	s_nop 0
	v_cvt_pk_bf16_f32 v12, v12, v13
	v_cvt_pk_bf16_f32 v13, v14, v15
	v_cvt_pk_bf16_f32 v14, v168, v169
	v_cvt_pk_bf16_f32 v15, v166, v167
	global_store_dwordx4 v[16:17], v[12:15], off
	v_pk_mul_f32 v[166:167], v[116:117], s[8:9] op_sel_hi:[1,0]
	v_pk_mul_f32 v[168:169], v[114:115], s[8:9] op_sel_hi:[1,0]
	v_pk_mul_f32 v[14:15], v[120:121], s[8:9] op_sel_hi:[1,0]
	v_pk_mul_f32 v[12:13], v[118:119], s[8:9] op_sel_hi:[1,0]
	s_nop 0
	v_cvt_pk_bf16_f32 v12, v12, v13
	v_cvt_pk_bf16_f32 v13, v14, v15
	v_cvt_pk_bf16_f32 v14, v168, v169
	v_cvt_pk_bf16_f32 v15, v166, v167
	global_store_dwordx4 v[16:17], v[12:15], off offset:256
	v_pk_mul_f32 v[166:167], v[108:109], s[8:9] op_sel_hi:[1,0]
	v_pk_mul_f32 v[168:169], v[106:107], s[8:9] op_sel_hi:[1,0]
	v_mad_i64_i32 v[12:13], s[24:25], v4, s50, v[6:7]
	v_lshl_add_u64 v[12:13], v[12:13], 0, s[22:23]
	v_lshl_add_u64 v[16:17], v[12:13], 0, v[154:155]
	v_pk_mul_f32 v[14:15], v[112:113], s[8:9] op_sel_hi:[1,0]
	v_pk_mul_f32 v[12:13], v[110:111], s[8:9] op_sel_hi:[1,0]
	s_nop 0
	v_cvt_pk_bf16_f32 v12, v12, v13
	v_cvt_pk_bf16_f32 v13, v14, v15
	v_cvt_pk_bf16_f32 v14, v168, v169
	v_cvt_pk_bf16_f32 v15, v166, v167
	global_store_dwordx4 v[16:17], v[12:15], off
	v_pk_mul_f32 v[166:167], v[100:101], s[8:9] op_sel_hi:[1,0]
	v_pk_mul_f32 v[168:169], v[98:99], s[8:9] op_sel_hi:[1,0]
	v_pk_mul_f32 v[14:15], v[104:105], s[8:9] op_sel_hi:[1,0]
	v_pk_mul_f32 v[12:13], v[102:103], s[8:9] op_sel_hi:[1,0]
	s_nop 0
	v_cvt_pk_bf16_f32 v12, v12, v13
	v_cvt_pk_bf16_f32 v13, v14, v15
	v_cvt_pk_bf16_f32 v14, v168, v169
	v_cvt_pk_bf16_f32 v15, v166, v167
	global_store_dwordx4 v[16:17], v[12:15], off offset:256
	v_pk_mul_f32 v[166:167], v[92:93], s[8:9] op_sel_hi:[1,0]
	v_pk_mul_f32 v[168:169], v[90:91], s[8:9] op_sel_hi:[1,0]
	v_mad_i64_i32 v[12:13], s[24:25], v2, s50, v[6:7]
	v_lshl_add_u64 v[12:13], v[12:13], 0, s[22:23]
	v_lshl_add_u64 v[16:17], v[12:13], 0, v[154:155]
	v_pk_mul_f32 v[14:15], v[96:97], s[8:9] op_sel_hi:[1,0]
	v_pk_mul_f32 v[12:13], v[94:95], s[8:9] op_sel_hi:[1,0]
	s_nop 0
	v_cvt_pk_bf16_f32 v12, v12, v13
	v_cvt_pk_bf16_f32 v13, v14, v15
	v_cvt_pk_bf16_f32 v14, v168, v169
	v_cvt_pk_bf16_f32 v15, v166, v167
	global_store_dwordx4 v[16:17], v[12:15], off
	v_pk_mul_f32 v[166:167], v[84:85], s[8:9] op_sel_hi:[1,0]
	v_pk_mul_f32 v[168:169], v[82:83], s[8:9] op_sel_hi:[1,0]
	v_pk_mul_f32 v[14:15], v[88:89], s[8:9] op_sel_hi:[1,0]
	v_pk_mul_f32 v[12:13], v[86:87], s[8:9] op_sel_hi:[1,0]
	s_nop 0
	v_cvt_pk_bf16_f32 v12, v12, v13
	v_cvt_pk_bf16_f32 v13, v14, v15
	v_cvt_pk_bf16_f32 v14, v168, v169
	v_cvt_pk_bf16_f32 v15, v166, v167
	global_store_dwordx4 v[16:17], v[12:15], off offset:256
	v_pk_mul_f32 v[166:167], v[76:77], s[8:9] op_sel_hi:[1,0]
	v_pk_mul_f32 v[168:169], v[74:75], s[8:9] op_sel_hi:[1,0]
	v_mad_i64_i32 v[12:13], s[24:25], v3, s50, v[6:7]
	v_lshl_add_u64 v[12:13], v[12:13], 0, s[22:23]
	v_lshl_add_u64 v[16:17], v[12:13], 0, v[154:155]
	v_pk_mul_f32 v[14:15], v[80:81], s[8:9] op_sel_hi:[1,0]
	v_pk_mul_f32 v[12:13], v[78:79], s[8:9] op_sel_hi:[1,0]
	v_add_u32_e32 v3, 0x90, v10
	v_cvt_pk_bf16_f32 v12, v12, v13
	v_cvt_pk_bf16_f32 v13, v14, v15
	v_cvt_pk_bf16_f32 v14, v168, v169
	v_cvt_pk_bf16_f32 v15, v166, v167
	global_store_dwordx4 v[16:17], v[12:15], off
	v_pk_mul_f32 v[166:167], v[68:69], s[8:9] op_sel_hi:[1,0]
	v_pk_mul_f32 v[168:169], v[66:67], s[8:9] op_sel_hi:[1,0]
	v_pk_mul_f32 v[14:15], v[72:73], s[8:9] op_sel_hi:[1,0]
	v_pk_mul_f32 v[12:13], v[70:71], s[8:9] op_sel_hi:[1,0]
	s_nop 0
	v_cvt_pk_bf16_f32 v12, v12, v13
	v_cvt_pk_bf16_f32 v13, v14, v15
	v_cvt_pk_bf16_f32 v14, v168, v169
	v_cvt_pk_bf16_f32 v15, v166, v167
	global_store_dwordx4 v[16:17], v[12:15], off offset:256
	v_pk_mul_f32 v[166:167], v[60:61], s[8:9] op_sel_hi:[1,0]
	v_pk_mul_f32 v[168:169], v[58:59], s[8:9] op_sel_hi:[1,0]
	v_mad_i64_i32 v[12:13], s[24:25], v3, s50, v[6:7]
	v_lshl_add_u64 v[12:13], v[12:13], 0, s[22:23]
	v_lshl_add_u64 v[16:17], v[12:13], 0, v[154:155]
	v_pk_mul_f32 v[14:15], v[64:65], s[8:9] op_sel_hi:[1,0]
	v_pk_mul_f32 v[12:13], v[62:63], s[8:9] op_sel_hi:[1,0]
	v_add_u32_e32 v3, 0xa0, v10
	v_cvt_pk_bf16_f32 v12, v12, v13
	v_cvt_pk_bf16_f32 v13, v14, v15
	v_cvt_pk_bf16_f32 v14, v168, v169
	v_cvt_pk_bf16_f32 v15, v166, v167
	global_store_dwordx4 v[16:17], v[12:15], off
	v_pk_mul_f32 v[166:167], v[48:49], s[8:9] op_sel_hi:[1,0]
	v_pk_mul_f32 v[168:169], v[46:47], s[8:9] op_sel_hi:[1,0]
	v_pk_mul_f32 v[14:15], v[56:57], s[8:9] op_sel_hi:[1,0]
	v_pk_mul_f32 v[12:13], v[54:55], s[8:9] op_sel_hi:[1,0]
	s_nop 0
	v_cvt_pk_bf16_f32 v12, v12, v13
	v_cvt_pk_bf16_f32 v13, v14, v15
	v_cvt_pk_bf16_f32 v14, v168, v169
	v_cvt_pk_bf16_f32 v15, v166, v167
	global_store_dwordx4 v[16:17], v[12:15], off offset:256
	v_pk_mul_f32 v[166:167], v[44:45], s[8:9] op_sel_hi:[1,0]
	v_pk_mul_f32 v[168:169], v[42:43], s[8:9] op_sel_hi:[1,0]
	v_mad_i64_i32 v[12:13], s[24:25], v3, s50, v[6:7]
	v_lshl_add_u64 v[12:13], v[12:13], 0, s[22:23]
	v_lshl_add_u64 v[16:17], v[12:13], 0, v[154:155]
	v_pk_mul_f32 v[14:15], v[52:53], s[8:9] op_sel_hi:[1,0]
	v_pk_mul_f32 v[12:13], v[50:51], s[8:9] op_sel_hi:[1,0]
	v_add_u32_e32 v3, 0xb0, v10
	v_cvt_pk_bf16_f32 v12, v12, v13
	v_cvt_pk_bf16_f32 v13, v14, v15
	v_cvt_pk_bf16_f32 v14, v168, v169
	v_cvt_pk_bf16_f32 v15, v166, v167
	global_store_dwordx4 v[16:17], v[12:15], off
	v_pk_mul_f32 v[166:167], v[32:33], s[8:9] op_sel_hi:[1,0]
	v_pk_mul_f32 v[168:169], v[30:31], s[8:9] op_sel_hi:[1,0]
	v_pk_mul_f32 v[14:15], v[40:41], s[8:9] op_sel_hi:[1,0]
	v_pk_mul_f32 v[12:13], v[38:39], s[8:9] op_sel_hi:[1,0]
	v_mad_i64_i32 v[6:7], s[24:25], v3, s50, v[6:7]
	v_cvt_pk_bf16_f32 v12, v12, v13
	v_cvt_pk_bf16_f32 v13, v14, v15
	v_cvt_pk_bf16_f32 v14, v168, v169
	v_cvt_pk_bf16_f32 v15, v166, v167
	global_store_dwordx4 v[16:17], v[12:15], off offset:256
	v_lshl_add_u64 v[6:7], v[6:7], 0, s[22:23]
	v_pk_mul_f32 v[16:17], v[28:29], s[8:9] op_sel_hi:[1,0]
	v_pk_mul_f32 v[14:15], v[36:37], s[8:9] op_sel_hi:[1,0]
	v_pk_mul_f32 v[12:13], v[34:35], s[8:9] op_sel_hi:[1,0]
	v_pk_mul_f32 v[166:167], v[26:27], s[8:9] op_sel_hi:[1,0]
	v_lshl_add_u64 v[6:7], v[6:7], 0, v[154:155]
	v_cvt_pk_bf16_f32 v12, v12, v13
	v_cvt_pk_bf16_f32 v13, v14, v15
	v_cvt_pk_bf16_f32 v14, v166, v167
	v_cvt_pk_bf16_f32 v15, v16, v17
	global_store_dwordx4 v[6:7], v[12:15], off
	v_pk_mul_f32 v[16:17], v[20:21], s[8:9] op_sel_hi:[1,0]
	v_pk_mul_f32 v[166:167], v[18:19], s[8:9] op_sel_hi:[1,0]
	v_pk_mul_f32 v[14:15], v[24:25], s[8:9] op_sel_hi:[1,0]
	v_pk_mul_f32 v[12:13], v[22:23], s[8:9] op_sel_hi:[1,0]
	s_mov_b64 s[22:23], 0
	v_cvt_pk_bf16_f32 v12, v12, v13
	v_cvt_pk_bf16_f32 v13, v14, v15
	v_cvt_pk_bf16_f32 v14, v166, v167
	v_cvt_pk_bf16_f32 v15, v16, v17
	global_store_dwordx4 v[6:7], v[12:15], off offset:256

.LBB0_1229:
	s_ashr_i32 s17, s16, 31
	v_cmp_lt_i64_e32 vcc, s[18:19], v[174:175]
	s_lshl_b64 s[18:19], s[16:17], 19
	v_readlane_b32 s6, v254, 36
	s_add_u32 s18, s6, s18
	v_readlane_b32 s6, v254, 37
	s_addc_u32 s19, s6, s19
	s_and_b64 s[20:21], vcc, exec
	s_cselect_b32 s6, s19, s25
	s_cselect_b32 s17, s18, s24
	s_ashr_i32 s15, s14, 31
	s_lshl_b64 s[20:21], s[14:15], 19
	s_add_u32 s20, s13, s20
	s_addc_u32 s21, s33, s21
	s_and_b64 s[28:29], vcc, exec
	s_cselect_b32 s15, s21, s27
	s_cselect_b32 s23, s20, s26
	s_add_u32 s24, s24, 0x40080
	s_addc_u32 s25, s25, 0
	s_add_u32 s30, s26, 0x100
	v_mov_b32_e32 v18, 0
	s_addc_u32 s31, s27, 0
	s_mov_b32 s48, -2
	v_mov_b32_e32 v19, v18
	v_mov_b32_e32 v20, v18
	v_mov_b32_e32 v21, v18
	v_mov_b32_e32 v22, v18
	v_mov_b32_e32 v23, v18
	v_mov_b32_e32 v24, v18
	v_mov_b32_e32 v25, v18
	v_mov_b32_e32 v34, v18
	v_mov_b32_e32 v35, v18
	v_mov_b32_e32 v36, v18
	v_mov_b32_e32 v37, v18
	v_mov_b32_e32 v38, v18
	v_mov_b32_e32 v39, v18
	v_mov_b32_e32 v40, v18
	v_mov_b32_e32 v41, v18
	v_mov_b32_e32 v50, v18
	v_mov_b32_e32 v51, v18
	v_mov_b32_e32 v52, v18
	v_mov_b32_e32 v53, v18
	v_mov_b32_e32 v54, v18
	v_mov_b32_e32 v55, v18
	v_mov_b32_e32 v56, v18
	v_mov_b32_e32 v57, v18
	v_mov_b32_e32 v66, v18
	v_mov_b32_e32 v67, v18
	v_mov_b32_e32 v68, v18
	v_mov_b32_e32 v69, v18
	v_mov_b32_e32 v70, v18
	v_mov_b32_e32 v71, v18
	v_mov_b32_e32 v72, v18
	v_mov_b32_e32 v73, v18
	v_mov_b32_e32 v26, v18
	v_mov_b32_e32 v27, v18
	v_mov_b32_e32 v28, v18
	v_mov_b32_e32 v29, v18
	v_mov_b32_e32 v30, v18
	v_mov_b32_e32 v31, v18
	v_mov_b32_e32 v32, v18
	v_mov_b32_e32 v33, v18
	v_mov_b32_e32 v42, v18
	v_mov_b32_e32 v43, v18
	v_mov_b32_e32 v44, v18
	v_mov_b32_e32 v45, v18
	v_mov_b32_e32 v46, v18
	v_mov_b32_e32 v47, v18
	v_mov_b32_e32 v48, v18
	v_mov_b32_e32 v49, v18
	v_mov_b32_e32 v58, v18
	v_mov_b32_e32 v59, v18
	v_mov_b32_e32 v60, v18
	v_mov_b32_e32 v61, v18
	v_mov_b32_e32 v62, v18
	v_mov_b32_e32 v63, v18
	v_mov_b32_e32 v64, v18
	v_mov_b32_e32 v65, v18
	v_mov_b32_e32 v74, v18
	v_mov_b32_e32 v75, v18
	v_mov_b32_e32 v76, v18
	v_mov_b32_e32 v77, v18
	v_mov_b32_e32 v78, v18
	v_mov_b32_e32 v79, v18
	v_mov_b32_e32 v80, v18
	v_mov_b32_e32 v81, v18
	v_mov_b32_e32 v82, v18
	v_mov_b32_e32 v83, v18
	v_mov_b32_e32 v84, v18
	v_mov_b32_e32 v85, v18
	v_mov_b32_e32 v86, v18
	v_mov_b32_e32 v87, v18
	v_mov_b32_e32 v88, v18
	v_mov_b32_e32 v89, v18
	v_mov_b32_e32 v98, v18
	v_mov_b32_e32 v99, v18
	v_mov_b32_e32 v100, v18
	v_mov_b32_e32 v101, v18
	v_mov_b32_e32 v102, v18
	v_mov_b32_e32 v103, v18
	v_mov_b32_e32 v104, v18
	v_mov_b32_e32 v105, v18
	v_mov_b32_e32 v114, v18
	v_mov_b32_e32 v115, v18
	v_mov_b32_e32 v116, v18
	v_mov_b32_e32 v117, v18
	v_mov_b32_e32 v118, v18
	v_mov_b32_e32 v119, v18
	v_mov_b32_e32 v120, v18
	v_mov_b32_e32 v121, v18
	v_mov_b32_e32 v130, v18
	v_mov_b32_e32 v131, v18
	v_mov_b32_e32 v132, v18
	v_mov_b32_e32 v133, v18
	v_mov_b32_e32 v134, v18
	v_mov_b32_e32 v135, v18
	v_mov_b32_e32 v136, v18
	v_mov_b32_e32 v137, v18
	v_mov_b32_e32 v90, v18
	v_mov_b32_e32 v91, v18
	v_mov_b32_e32 v92, v18
	v_mov_b32_e32 v93, v18
	v_mov_b32_e32 v94, v18
	v_mov_b32_e32 v95, v18
	v_mov_b32_e32 v96, v18
	v_mov_b32_e32 v97, v18
	v_mov_b32_e32 v106, v18
	v_mov_b32_e32 v107, v18
	v_mov_b32_e32 v108, v18
	v_mov_b32_e32 v109, v18
	v_mov_b32_e32 v110, v18
	v_mov_b32_e32 v111, v18
	v_mov_b32_e32 v112, v18
	v_mov_b32_e32 v113, v18
	v_mov_b32_e32 v122, v18
	v_mov_b32_e32 v123, v18
	v_mov_b32_e32 v124, v18
	v_mov_b32_e32 v125, v18
	v_mov_b32_e32 v126, v18
	v_mov_b32_e32 v127, v18
	v_mov_b32_e32 v128, v18
	v_mov_b32_e32 v129, v18
	v_mov_b32_e32 v138, v18
	v_mov_b32_e32 v139, v18
	v_mov_b32_e32 v140, v18
	v_mov_b32_e32 v141, v18
	v_mov_b32_e32 v142, v18
	v_mov_b32_e32 v143, v18
	v_mov_b32_e32 v144, v18
	v_mov_b32_e32 v145, v18
	v_add_u32_e32 v184, 0x18000, v186
	v_add_u32_e32 v185, 0x1c000, v186
.LBB0_1230:
	ds_read_b128 v[2:5], v190
	ds_read_b128 v[6:9], v190 offset:1024
	ds_read_b128 v[10:13], v190 offset:2048
	ds_read_b128 v[14:17], v190 offset:3072
	s_add_u32 s26, s24, 0xfffc0080
	s_addc_u32 s27, s25, -1
	s_cmp_eq_u32 s48, 12
	s_cselect_b32 s29, s6, s27
	s_cselect_b32 s28, s17, s26
	s_cselect_b32 s27, s15, s31
	s_cselect_b32 s26, s23, s30
	s_add_i32 m0, s35, 0xc000
	ds_read_b128 v[194:197], v191
	ds_read_b128 v[198:201], v191 offset:1024
	ds_read_b128 v[214:217], v191 offset:2048
	ds_read_b128 v[218:221], v191 offset:3072
	ds_read_b128 v[222:225], v191 offset:4096
	ds_read_b128 v[226:229], v191 offset:5120
	ds_read_b128 v[230:233], v191 offset:6144
	ds_read_b128 v[234:237], v191 offset:7168
	global_load_lds_dwordx4 v170, s[24:25]
	s_add_i32 m0, s35, 0xe000
	s_nop 0
	global_load_lds_dwordx4 v172, s[24:25]
	s_waitcnt lgkmcnt(8)
	s_barrier
	s_waitcnt lgkmcnt(0)
	s_setprio 1
	s_waitcnt lgkmcnt(0)
	v_mfma_scale_f32_16x16x128_f8f6f4 v[142:145], v[2:9], v[194:201], v[142:145], v192, v192 op_sel_hi:[0,0,0]
	v_mfma_scale_f32_16x16x128_f8f6f4 v[138:141], v[10:17], v[194:201], v[138:141], v192, v192 op_sel_hi:[0,0,0]
	v_mfma_scale_f32_16x16x128_f8f6f4 v[126:129], v[2:9], v[214:221], v[126:129], v192, v192 op_sel_hi:[0,0,0]
	v_mfma_scale_f32_16x16x128_f8f6f4 v[122:125], v[10:17], v[214:221], v[122:125], v192, v192 op_sel_hi:[0,0,0]
	v_mfma_scale_f32_16x16x128_f8f6f4 v[110:113], v[2:9], v[222:229], v[110:113], v192, v192 op_sel_hi:[0,0,0]
	v_mfma_scale_f32_16x16x128_f8f6f4 v[106:109], v[10:17], v[222:229], v[106:109], v192, v192 op_sel_hi:[0,0,0]
	v_mfma_scale_f32_16x16x128_f8f6f4 v[94:97], v[2:9], v[230:237], v[94:97], v192, v192 op_sel_hi:[0,0,0]
	v_mfma_scale_f32_16x16x128_f8f6f4 v[90:93], v[10:17], v[230:237], v[90:93], v192, v192 op_sel_hi:[0,0,0]
	s_setprio 0
	s_barrier
	s_add_i32 s49, s44, s34
	s_add_u32 s66, s26, 0x80
	s_addc_u32 s67, s27, 0
	s_mov_b32 m0, s49
	ds_read_b128 v[238:241], v193
	ds_read_b128 v[242:245], v193 offset:1024
	ds_read_b128 v[246:249], v193 offset:2048
	ds_read_b128 v[250:253], v193 offset:3072
	global_load_lds_dwordx4 v148, s[26:27]
	s_add_i32 m0, s49, 0x2000
	s_nop 0
	global_load_lds_dwordx4 v152, s[26:27]
	s_barrier
	s_waitcnt lgkmcnt(0)
	s_setprio 1
	s_waitcnt lgkmcnt(0)
	v_mfma_scale_f32_16x16x128_f8f6f4 v[134:137], v[238:245], v[194:201], v[134:137], v192, v192 op_sel_hi:[0,0,0]
	v_mfma_scale_f32_16x16x128_f8f6f4 v[130:133], v[246:253], v[194:201], v[130:133], v192, v192 op_sel_hi:[0,0,0]
	v_mfma_scale_f32_16x16x128_f8f6f4 v[118:121], v[238:245], v[214:221], v[118:121], v192, v192 op_sel_hi:[0,0,0]
	v_mfma_scale_f32_16x16x128_f8f6f4 v[114:117], v[246:253], v[214:221], v[114:117], v192, v192 op_sel_hi:[0,0,0]
	v_mfma_scale_f32_16x16x128_f8f6f4 v[102:105], v[238:245], v[222:229], v[102:105], v192, v192 op_sel_hi:[0,0,0]
	v_mfma_scale_f32_16x16x128_f8f6f4 v[98:101], v[246:253], v[222:229], v[98:101], v192, v192 op_sel_hi:[0,0,0]
	v_mfma_scale_f32_16x16x128_f8f6f4 v[86:89], v[238:245], v[230:237], v[86:89], v192, v192 op_sel_hi:[0,0,0]
	v_mfma_scale_f32_16x16x128_f8f6f4 v[82:85], v[246:253], v[230:237], v[82:85], v192, v192 op_sel_hi:[0,0,0]
	s_setprio 0
	s_mov_b32 m0, s35
	s_add_u32 s68, s28, 0x80
	s_addc_u32 s69, s29, 0
	s_barrier
	ds_read_b128 v[194:197], v191 offset:16384
	ds_read_b128 v[198:201], v191 offset:17408
	ds_read_b128 v[214:217], v191 offset:18432
	ds_read_b128 v[218:221], v191 offset:19456
	ds_read_b128 v[222:225], v191 offset:20480
	ds_read_b128 v[226:229], v191 offset:21504
	ds_read_b128 v[230:233], v191 offset:22528
	ds_read_b128 v[234:237], v191 offset:23552
	global_load_lds_dwordx4 v146, s[28:29]
	s_mov_b32 m0, s36
	s_nop 0
	global_load_lds_dwordx4 v150, s[28:29]
	s_barrier
	s_waitcnt lgkmcnt(0)
	s_setprio 1
	s_waitcnt lgkmcnt(0)
	v_mfma_scale_f32_16x16x128_f8f6f4 v[78:81], v[2:9], v[194:201], v[78:81], v192, v192 op_sel_hi:[0,0,0]
	v_mfma_scale_f32_16x16x128_f8f6f4 v[74:77], v[10:17], v[194:201], v[74:77], v192, v192 op_sel_hi:[0,0,0]
	v_mfma_scale_f32_16x16x128_f8f6f4 v[62:65], v[2:9], v[214:221], v[62:65], v192, v192 op_sel_hi:[0,0,0]
	v_mfma_scale_f32_16x16x128_f8f6f4 v[58:61], v[10:17], v[214:221], v[58:61], v192, v192 op_sel_hi:[0,0,0]
	v_mfma_scale_f32_16x16x128_f8f6f4 v[46:49], v[2:9], v[222:229], v[46:49], v192, v192 op_sel_hi:[0,0,0]
	v_mfma_scale_f32_16x16x128_f8f6f4 v[42:45], v[10:17], v[222:229], v[42:45], v192, v192 op_sel_hi:[0,0,0]
	v_mfma_scale_f32_16x16x128_f8f6f4 v[30:33], v[2:9], v[230:237], v[30:33], v192, v192 op_sel_hi:[0,0,0]
	v_mfma_scale_f32_16x16x128_f8f6f4 v[26:29], v[10:17], v[230:237], v[26:29], v192, v192 op_sel_hi:[0,0,0]
	s_setprio 0
	s_barrier
	s_add_u32 s50, s26, 0x40000
	s_addc_u32 s51, s27, 0
	s_add_i32 s49, s45, s34
	s_mov_b32 m0, s49
	s_nop 0
	global_load_lds_dwordx4 v148, s[50:51]
	s_add_i32 m0, s49, 0x2000
	s_nop 0
	global_load_lds_dwordx4 v152, s[50:51]
	s_waitcnt vmcnt(6)
	s_barrier
	s_setprio 1
	v_mfma_scale_f32_16x16x128_f8f6f4 v[70:73], v[238:245], v[194:201], v[70:73], v192, v192 op_sel_hi:[0,0,0]
	v_mfma_scale_f32_16x16x128_f8f6f4 v[66:69], v[246:253], v[194:201], v[66:69], v192, v192 op_sel_hi:[0,0,0]
	v_mfma_scale_f32_16x16x128_f8f6f4 v[54:57], v[238:245], v[214:221], v[54:57], v192, v192 op_sel_hi:[0,0,0]
	v_mfma_scale_f32_16x16x128_f8f6f4 v[50:53], v[246:253], v[214:221], v[50:53], v192, v192 op_sel_hi:[0,0,0]
	v_mfma_scale_f32_16x16x128_f8f6f4 v[38:41], v[238:245], v[222:229], v[38:41], v192, v192 op_sel_hi:[0,0,0]
	v_mfma_scale_f32_16x16x128_f8f6f4 v[34:37], v[246:253], v[222:229], v[34:37], v192, v192 op_sel_hi:[0,0,0]
	v_mfma_scale_f32_16x16x128_f8f6f4 v[22:25], v[238:245], v[230:237], v[22:25], v192, v192 op_sel_hi:[0,0,0]
	v_mfma_scale_f32_16x16x128_f8f6f4 v[18:21], v[246:253], v[230:237], v[18:21], v192, v192 op_sel_hi:[0,0,0]
	s_setprio 0
	s_add_i32 s49, 0, 0x18000
	s_barrier
	ds_read_b128 v[2:5], v184
	ds_read_b128 v[6:9], v184 offset:1024
	ds_read_b128 v[10:13], v184 offset:2048
	ds_read_b128 v[14:17], v184 offset:3072
	s_add_u32 s28, s28, 0x40000
	s_addc_u32 s29, s29, 0
	s_mov_b32 m0, s37
	ds_read_b128 v[194:197], v191 offset:32768
	ds_read_b128 v[198:201], v191 offset:33792
	ds_read_b128 v[214:217], v191 offset:34816
	ds_read_b128 v[218:221], v191 offset:35840
	ds_read_b128 v[222:225], v191 offset:36864
	ds_read_b128 v[226:229], v191 offset:37888
	ds_read_b128 v[230:233], v191 offset:38912
	ds_read_b128 v[234:237], v191 offset:39936
	global_load_lds_dwordx4 v146, s[28:29]
	s_mov_b32 m0, s38
	s_nop 0
	global_load_lds_dwordx4 v150, s[28:29]
	s_waitcnt lgkmcnt(8)
	s_barrier
	s_waitcnt lgkmcnt(0)
	s_setprio 1
	s_waitcnt lgkmcnt(0)
	v_mfma_scale_f32_16x16x128_f8f6f4 v[142:145], v[2:9], v[194:201], v[142:145], v192, v192 op_sel_hi:[0,0,0]
	v_mfma_scale_f32_16x16x128_f8f6f4 v[138:141], v[10:17], v[194:201], v[138:141], v192, v192 op_sel_hi:[0,0,0]
	v_mfma_scale_f32_16x16x128_f8f6f4 v[126:129], v[2:9], v[214:221], v[126:129], v192, v192 op_sel_hi:[0,0,0]
	v_mfma_scale_f32_16x16x128_f8f6f4 v[122:125], v[10:17], v[214:221], v[122:125], v192, v192 op_sel_hi:[0,0,0]
	v_mfma_scale_f32_16x16x128_f8f6f4 v[110:113], v[2:9], v[222:229], v[110:113], v192, v192 op_sel_hi:[0,0,0]
	v_mfma_scale_f32_16x16x128_f8f6f4 v[106:109], v[10:17], v[222:229], v[106:109], v192, v192 op_sel_hi:[0,0,0]
	v_mfma_scale_f32_16x16x128_f8f6f4 v[94:97], v[2:9], v[230:237], v[94:97], v192, v192 op_sel_hi:[0,0,0]
	v_mfma_scale_f32_16x16x128_f8f6f4 v[90:93], v[10:17], v[230:237], v[90:93], v192, v192 op_sel_hi:[0,0,0]
	s_setprio 0
	s_barrier
	s_add_i32 s28, 0, 0x1c000
	s_add_i32 s29, s49, s34
	s_mov_b32 m0, s29
	ds_read_b128 v[238:241], v185
	ds_read_b128 v[242:245], v185 offset:1024
	ds_read_b128 v[246:249], v185 offset:2048
	ds_read_b128 v[250:253], v185 offset:3072
	global_load_lds_dwordx4 v148, s[66:67]
	s_add_i32 m0, s29, 0x2000
	s_nop 0
	global_load_lds_dwordx4 v152, s[66:67]
	s_barrier
	s_waitcnt lgkmcnt(0)
	s_setprio 1
	s_waitcnt lgkmcnt(0)
	v_mfma_scale_f32_16x16x128_f8f6f4 v[134:137], v[238:245], v[194:201], v[134:137], v192, v192 op_sel_hi:[0,0,0]
	v_mfma_scale_f32_16x16x128_f8f6f4 v[130:133], v[246:253], v[194:201], v[130:133], v192, v192 op_sel_hi:[0,0,0]
	v_mfma_scale_f32_16x16x128_f8f6f4 v[118:121], v[238:245], v[214:221], v[118:121], v192, v192 op_sel_hi:[0,0,0]
	v_mfma_scale_f32_16x16x128_f8f6f4 v[114:117], v[246:253], v[214:221], v[114:117], v192, v192 op_sel_hi:[0,0,0]
	v_mfma_scale_f32_16x16x128_f8f6f4 v[102:105], v[238:245], v[222:229], v[102:105], v192, v192 op_sel_hi:[0,0,0]
	v_mfma_scale_f32_16x16x128_f8f6f4 v[98:101], v[246:253], v[222:229], v[98:101], v192, v192 op_sel_hi:[0,0,0]
	v_mfma_scale_f32_16x16x128_f8f6f4 v[86:89], v[238:245], v[230:237], v[86:89], v192, v192 op_sel_hi:[0,0,0]
	v_mfma_scale_f32_16x16x128_f8f6f4 v[82:85], v[246:253], v[230:237], v[82:85], v192, v192 op_sel_hi:[0,0,0]
	s_setprio 0
	s_mov_b32 m0, s41
	s_barrier
	ds_read_b128 v[194:197], v191 offset:49152
	ds_read_b128 v[198:201], v191 offset:50176
	ds_read_b128 v[214:217], v191 offset:51200
	ds_read_b128 v[218:221], v191 offset:52224
	ds_read_b128 v[222:225], v191 offset:53248
	ds_read_b128 v[226:229], v191 offset:54272
	ds_read_b128 v[230:233], v191 offset:55296
	ds_read_b128 v[234:237], v191 offset:56320
	global_load_lds_dwordx4 v146, s[68:69]
	s_mov_b32 m0, s42
	s_nop 0
	global_load_lds_dwordx4 v150, s[68:69]
	s_barrier
	s_waitcnt lgkmcnt(0)
	s_setprio 1
	s_waitcnt lgkmcnt(0)
	v_mfma_scale_f32_16x16x128_f8f6f4 v[78:81], v[2:9], v[194:201], v[78:81], v192, v192 op_sel_hi:[0,0,0]
	v_mfma_scale_f32_16x16x128_f8f6f4 v[74:77], v[10:17], v[194:201], v[74:77], v192, v192 op_sel_hi:[0,0,0]
	v_mfma_scale_f32_16x16x128_f8f6f4 v[62:65], v[2:9], v[214:221], v[62:65], v192, v192 op_sel_hi:[0,0,0]
	v_mfma_scale_f32_16x16x128_f8f6f4 v[58:61], v[10:17], v[214:221], v[58:61], v192, v192 op_sel_hi:[0,0,0]
	v_mfma_scale_f32_16x16x128_f8f6f4 v[46:49], v[2:9], v[222:229], v[46:49], v192, v192 op_sel_hi:[0,0,0]
	v_mfma_scale_f32_16x16x128_f8f6f4 v[42:45], v[10:17], v[222:229], v[42:45], v192, v192 op_sel_hi:[0,0,0]
	v_mfma_scale_f32_16x16x128_f8f6f4 v[30:33], v[2:9], v[230:237], v[30:33], v192, v192 op_sel_hi:[0,0,0]
	v_mfma_scale_f32_16x16x128_f8f6f4 v[26:29], v[10:17], v[230:237], v[26:29], v192, v192 op_sel_hi:[0,0,0]
	s_setprio 0
	s_barrier
	s_add_u32 s26, s26, 0x40080
	s_addc_u32 s27, s27, 0
	s_add_i32 s28, s28, s34
	s_mov_b32 m0, s28
	s_nop 0
	global_load_lds_dwordx4 v148, s[26:27]
	s_add_i32 m0, s28, 0x2000
	s_nop 0
	global_load_lds_dwordx4 v152, s[26:27]
	s_waitcnt vmcnt(6)
	s_barrier
	s_setprio 1
	v_mfma_scale_f32_16x16x128_f8f6f4 v[70:73], v[238:245], v[194:201], v[70:73], v192, v192 op_sel_hi:[0,0,0]
	v_mfma_scale_f32_16x16x128_f8f6f4 v[66:69], v[246:253], v[194:201], v[66:69], v192, v192 op_sel_hi:[0,0,0]
	v_mfma_scale_f32_16x16x128_f8f6f4 v[54:57], v[238:245], v[214:221], v[54:57], v192, v192 op_sel_hi:[0,0,0]
	v_mfma_scale_f32_16x16x128_f8f6f4 v[50:53], v[246:253], v[214:221], v[50:53], v192, v192 op_sel_hi:[0,0,0]
	v_mfma_scale_f32_16x16x128_f8f6f4 v[38:41], v[238:245], v[222:229], v[38:41], v192, v192 op_sel_hi:[0,0,0]
	v_mfma_scale_f32_16x16x128_f8f6f4 v[34:37], v[246:253], v[222:229], v[34:37], v192, v192 op_sel_hi:[0,0,0]
	v_mfma_scale_f32_16x16x128_f8f6f4 v[22:25], v[238:245], v[230:237], v[22:25], v192, v192 op_sel_hi:[0,0,0]
	v_mfma_scale_f32_16x16x128_f8f6f4 v[18:21], v[246:253], v[230:237], v[18:21], v192, v192 op_sel_hi:[0,0,0]
	s_setprio 0
	s_add_i32 s48, s48, 2
	s_add_u32 s24, s24, 0x100
	s_addc_u32 s25, s25, 0
	s_add_u32 s30, s30, 0x100
	s_addc_u32 s31, s31, 0
	s_cmp_gt_u32 s48, 13
	s_barrier
	s_cbranch_scc0 .LBB0_1230
	s_lshl_b32 s26, s22, 8
	s_cmpk_gt_i32 s22, 0x7f
	s_mov_b64 s[30:31], -1
	s_cbranch_scc0 .LBB0_1233
	s_add_i32 s6, s26, 0xffff8000
	s_mov_b32 s27, s7
	s_lshl_b64 s[28:29], s[6:7], 12
	s_lshl_b64 s[24:25], s[26:27], 12
	s_mov_b64 s[30:31], 0
